# attn: key-tile rotation (2qb+11head)&31
# baseline (speedup 1.0000x reference)
.Lp_top:
	s_lshl_b32 s6, s21, 20
	s_add_u32 s4, s4, s6
	s_addc_u32 s5, s5, 0
	v_lshlrev_b32_e32 v54, 4, v0
	v_mov_b32_e32 v55, v63
	s_lshl_b32 s3, s3, 1
	s_mul_i32 s20, s21, 11
	v_lshl_add_u64 v[4:5], s[4:5], 0, v[54:55]
	s_mov_b64 s[4:5], 0x1000000
	s_add_i32 s20, s20, s3
	v_lshl_add_u64 v[170:171], v[4:5], 0, s[4:5]
	s_and_b32 s22, s20, 31
	s_lshl_b32 s4, s20, 12
	s_lshl_b32 s12, s22, 13
	s_add_i32 s5, s4, 0x1000
	v_lshl_add_u64 v[58:59], v[170:171], 0, s[12:13]
	s_mov_b32 s3, 0x80000
	s_and_b32 s5, s5, 0x1f000
	v_add_co_u32_e32 v16, vcc, s3, v58
	s_lshl_b32 s12, s5, 1
	s_nop 0
	v_addc_co_u32_e32 v17, vcc, 0, v59, vcc
	v_lshl_add_u64 v[56:57], v[170:171], 0, s[12:13]
	global_load_dwordx4 v[4:7], v[58:59], off
	global_load_dwordx4 v[8:11], v[56:57], off
	global_load_dwordx4 v[12:15], v[16:17], off
	v_add_co_u32_e32 v16, vcc, s3, v56
	v_lshrrev_b32_e32 v184, 8, v0
	s_nop 0
	v_addc_co_u32_e32 v17, vcc, 0, v57, vcc
	global_load_dwordx4 v[16:19], v[16:17], off
	v_and_b32_e32 v20, 19, v0
	v_lshlrev_b32_e32 v21, 1, v0
	v_and_b32_e32 v2, 4, v2
	v_and_or_b32 v20, v21, 8, v20
	v_lshlrev_b32_e32 v101, 5, v184
	s_addk_i32 s4, 0x2000
	v_or3_b32 v2, v20, v2, v101
	s_and_b32 s4, s4, 0x1f000
	v_mul_u32_u24_e32 v2, 0x48, v2
	s_lshl_b32 s12, s4, 1
	v_lshlrev_b32_e32 v3, 3, v0
	v_lshlrev_b32_e32 v100, 1, v99
	v_lshlrev_b32_e32 v2, 1, v2
	v_lshl_add_u64 v[60:61], v[170:171], 0, s[12:13]
	v_and_b32_e32 v3, 56, v3
	v_add3_u32 v186, 0, v2, v100
	v_add_co_u32_e32 v2, vcc, s3, v60
	v_lshlrev_b32_e32 v68, 1, v3
	s_nop 0
	v_addc_co_u32_e32 v3, vcc, 0, v61, vcc
	global_load_dwordx4 v[162:165], v[60:61], off
	global_load_dwordx4 v[166:169], v[2:3], off
	v_lshrrev_b32_e32 v82, 3, v0
	v_mul_u32_u24_e32 v22, 0x48, v82
	v_lshlrev_b32_e32 v21, 1, v22
	v_add3_u32 v185, 0, v21, v68
	s_mov_b64 s[24:25], 0x80000
	s_add_i32 s17, s20, 3
	s_add_i32 s18, s20, 4
	v_mov_b32_e32 v62, v63
	v_lshrrev_b32_e32 v55, 6, v0
	v_mov_b32_e32 v83, 0
	v_mov_b32_e32 v84, 0
	v_lshl_add_u64 v[70:71], v[58:59], 0, s[24:25]
	v_lshl_add_u64 v[66:67], v[56:57], 0, s[24:25]
	v_lshl_add_u64 v[64:65], v[60:61], 0, s[24:25]
	s_waitcnt vmcnt(5)
	ds_write_b128 v185, v[4:7]
	s_waitcnt vmcnt(3)
	ds_write_b128 v185, v[12:15] offset:9216
	ds_write_b128 v185, v[8:11] offset:18432
	s_waitcnt vmcnt(2)
	ds_write_b128 v185, v[16:19] offset:27648
	s_waitcnt lgkmcnt(0)
	s_barrier
	ds_read_b128 v[2:5], v186
	ds_read_b128 v[38:41], v186 offset:32
	s_waitcnt lgkmcnt(1)
	v_mfma_f32_32x32x16_f16 v[2:17], v[2:5], v[114:117], 0
	ds_read_b128 v[18:21], v186 offset:9216
	ds_read_b128 v[46:49], v186 offset:9248
	s_waitcnt lgkmcnt(1)
	v_mfma_f32_32x32x16_f16 v[18:33], v[18:21], v[130:133], 0
	v_mfma_f32_32x32x16_f16 v[2:17], v[38:41], v[118:121], v[2:17]
	s_waitcnt lgkmcnt(0)
	v_mfma_f32_32x32x16_f16 v[18:33], v[46:49], v[134:137], v[18:33]
	ds_read_b128 v[38:41], v186 offset:64
	ds_read_b128 v[46:49], v186 offset:96
	s_waitcnt lgkmcnt(1)
	v_mfma_f32_32x32x16_f16 v[2:17], v[38:41], v[122:125], v[2:17]
	ds_read_b128 v[38:41], v186 offset:9280
	ds_read_b128 v[50:53], v186 offset:9312
	s_load_dwordx4 s[4:7], s[0:1], 0x38
	s_load_dwordx2 s[14:15], s[0:1], 0x8
	s_mov_b32 s0, -2
	s_mov_b32 s1, 0x3f800000
	s_waitcnt lgkmcnt(0)
	s_barrier
	v_mfma_f32_32x32x16_f16 v[18:33], v[38:41], v[138:141], v[18:33]
	v_mfma_f32_32x32x16_f16 v[2:17], v[46:49], v[126:129], v[2:17]
	v_mfma_f32_32x32x16_f16 v[18:33], v[50:53], v[142:145], v[18:33]
	s_lshl_b32 s12, s17, 13
	s_and_b32 s12, s12, 0x3e000
	s_add_u32 s28, s12, s3
	s_mov_b32 s29, 0
	v_lshl_add_u64 v[176:177], v[170:171], 0, s[12:13]
	global_load_dwordx4 v[50:53], v[176:177], off
	v_lshl_add_u64 v[176:177], v[170:171], 0, s[28:29]
	global_load_dwordx4 v[94:97], v[176:177], off
	s_nop 7
	s_cmp_eq_u32 s37, 1
	s_cbranch_scc0 .Lf_A
	v_mov_b32_e32 v83, 0xf149f2ca
	v_mov_b32_e32 v84, 0xf149f2ca
	s_branch .Ls_A

.Ll1_cont:
	ds_bpermute_b32 v2, v69, v84
	ds_bpermute_b32 v5, v69, v83
	v_max_f32_e32 v4, v84, v84
	v_max_f32_e32 v7, v83, v83
	ds_bpermute_b32 v3, v69, v63
	s_waitcnt lgkmcnt(2)
	v_max_f32_e32 v6, v2, v2
	v_max_f32_e32 v4, v4, v6
	v_sub_f32_e32 v6, v84, v4
	v_exp_f32_e32 v9, v6
	s_waitcnt lgkmcnt(1)
	v_max_f32_e32 v6, v5, v5
	v_sub_f32_e32 v2, v2, v4
	v_max_f32_e32 v6, v7, v6
	v_exp_f32_e32 v11, v2
	ds_bpermute_b32 v2, v69, v62
	v_sub_f32_e32 v5, v5, v6
	v_sub_f32_e32 v7, v83, v6
	v_exp_f32_e32 v10, v5
	v_exp_f32_e32 v8, v7
	v_cmp_gt_u32_e32 vcc, 32, v98
	s_waitcnt lgkmcnt(0)
	v_pk_mul_f32 v[2:3], v[10:11], v[2:3]
	s_nop 0
	v_pk_fma_f32 v[8:9], v[62:63], v[8:9], v[2:3]
	v_lshlrev_b32_e32 v2, 7, v184
	v_or3_b32 v10, v183, v2, v1
	s_and_saveexec_b64 s[0:1], vcc
	v_lshl_add_u32 v2, v10, 4, 0
	v_add_u32_e32 v2, 0x21000, v2
	v_mov_b32_e32 v5, v9
	v_mov_b32_e32 v7, v8
	ds_write_b128 v2, v[4:7]
	s_or_b64 exec, exec, s[0:1]
	s_lshl_b32 s12, s21, 7
	s_mov_b32 s3, 0
	v_or_b32_e32 v2, s12, v82
	s_lshl_b32 s13, s21, 11
	s_add_i32 s23, 0, 0x12000
	v_lshlrev_b32_e32 v2, 12, v2
	v_mov_b32_e32 v3, 0
	s_add_i32 s13, s13, s16
	s_lshl_b64 s[0:1], s[2:3], 13
	v_lshl_add_u64 v[12:13], s[14:15], 0, v[2:3]
	v_mov_b32_e32 v69, v3
	s_add_u32 s0, s10, s0
	v_lshl_add_u64 v[172:173], v[12:13], 0, v[68:69]
	s_addc_u32 s1, s11, s1
	s_lshl_b32 s10, s22, 7
	s_mov_b32 s11, s3
	s_waitcnt vmcnt(1)
	v_lshl_add_u64 v[36:37], v[172:173], 0, s[10:11]
	s_mov_b32 s10, 0x40000
	v_add_co_u32_e32 v38, vcc, s10, v36
	s_waitcnt lgkmcnt(0)
	s_barrier
	global_load_dwordx4 v[12:15], v[58:59], off
	global_load_dwordx4 v[16:19], v[70:71], off
	v_addc_co_u32_e32 v39, vcc, 0, v37, vcc
	global_load_dwordx4 v[20:23], v[56:57], off
	global_load_dwordx4 v[24:27], v[66:67], off
	global_load_dwordx4 v[28:31], v[36:37], off
	global_load_dwordx4 v[32:35], v[38:39], off
	v_add_f32_e32 v2, v78, v80
	s_movk_i32 s11, 0x1200
	v_add_f32_e32 v5, v79, v81
	s_mov_b32 s14, 0x3fb8aa3b
	v_lshlrev_b32_e32 v10, 4, v10
	v_mov_b32_e32 v36, s23
	v_mul_f32_e32 v37, 0x3fb8aa3b, v2
	v_mul_f32_e32 v38, 0x3fb8aa3b, v5
	v_xor_b32_e32 v10, 0x800, v10
	v_mad_u32_u24 v40, v55, s11, v36
	v_fma_f32 v36, v2, s14, -v37
	v_rndne_f32_e32 v39, v37
	v_fma_f32 v41, v5, s14, -v38
	s_waitcnt vmcnt(6)
	v_rndne_f32_e32 v42, v38
	v_add_u32_e32 v10, 0, v10
	v_fmac_f32_e32 v36, 0x32a5705f, v2
	v_sub_f32_e32 v37, v37, v39
	v_fmac_f32_e32 v41, 0x32a5705f, v5
	v_sub_f32_e32 v38, v38, v42
	v_add_u32_e32 v10, 0x21000, v10
	v_add_f32_e32 v44, v37, v36
	global_load_dwordx4 v[146:149], v[60:61], off
	global_load_dwordx4 v[150:153], v[64:65], off
	v_cvt_i32_f32_e32 v43, v39
	v_add_f32_e32 v41, v38, v41
	ds_read_b128 v[36:39], v10
	v_exp_f32_e32 v10, v44
	v_cvt_i32_f32_e32 v42, v42
	v_exp_f32_e32 v41, v41
	s_mov_b32 s21, 0xc2ce8ed0
	s_lshl_b32 s11, s20, 6
	s_add_i32 s14, s11, 64
	v_ldexp_f32 v10, v10, v43
	v_cmp_ngt_f32_e32 vcc, s21, v2
	s_mov_b32 s22, 0x42b17218
	s_and_b32 s14, s14, 0x7c0
	v_ldexp_f32 v41, v41, v42
	v_cndmask_b32_e32 v10, 0, v10, vcc
	v_cmp_ngt_f32_e32 vcc, s21, v5
	v_mov_b32_e32 v7, 0x7f800000
	v_max_f32_e32 v11, v4, v4
	s_mov_b32 s15, s3
	s_lshl_b32 s14, s14, 1
	s_waitcnt lgkmcnt(0)
	v_max_f32_e32 v42, v36, v36
	v_cndmask_b32_e32 v41, 0, v41, vcc
	v_cmp_nlt_f32_e32 vcc, s22, v2
	v_max_f32_e32 v187, v11, v42
	v_mov_b32_e32 v55, v3
	v_cndmask_b32_e32 v2, v7, v10, vcc
	v_cmp_nlt_f32_e32 vcc, s22, v5
	v_lshl_add_u64 v[10:11], v[172:173], 0, s[14:15]
	v_lshl_add_u64 v[178:179], s[0:1], 0, v[54:55]
	v_cndmask_b32_e32 v5, v7, v41, vcc
	v_sub_f32_e32 v2, v2, v5
	v_add_f32_e32 v41, 0x3e4ccccd, v2
	v_sub_f32_e32 v2, v4, v187
	v_max_f32_e32 v4, v6, v6
	s_and_b32 s1, s2, 7
	s_mulk_i32 s1, 0x580
	s_mulk_i32 s19, 0x2c0
	s_add_i32 s0, s20, 2
	s_waitcnt vmcnt(7)
	ds_write_b128 v185, v[12:15]
	s_waitcnt vmcnt(6)
	ds_write_b128 v185, v[16:19] offset:9216
	s_waitcnt vmcnt(5)
	ds_write_b128 v185, v[20:23] offset:18432
	s_waitcnt vmcnt(4)
	ds_write_b128 v185, v[24:27] offset:27648
	s_waitcnt vmcnt(3)
	ds_write_b128 v185, v[28:31] offset:36864
	s_waitcnt vmcnt(2)
	ds_write_b128 v185, v[32:35] offset:46080
	v_add_co_u32_e32 v12, vcc, s10, v10
	v_exp_f32_e32 v23, v2
	s_nop 0
	v_addc_co_u32_e32 v13, vcc, 0, v11, vcc
	global_load_dwordx4 v[154:157], v[10:11], off
	global_load_dwordx4 v[158:161], v[12:13], off
	s_waitcnt lgkmcnt(0)
	s_barrier
	ds_read_b128 v[10:13], v186
	v_sub_f32_e32 v2, v36, v187
	v_exp_f32_e32 v25, v2
	v_max_f32_e32 v2, v38, v38
	v_max_f32_e32 v188, v4, v2
	v_sub_f32_e32 v2, v6, v188
	v_exp_f32_e32 v22, v2
	v_sub_f32_e32 v2, v38, v188
	v_exp_f32_e32 v24, v2
	ds_read_b128 v[14:17], v186 offset:9216
	ds_read_b128 v[18:21], v186 offset:32
	s_waitcnt lgkmcnt(2)
	v_mfma_f32_32x32x16_f16 v[66:81], v[10:13], v[114:117], 0
	v_mov_b32_e32 v36, v39
	v_mul_f32_e64 v10, v36, v24
	v_mul_f32_e64 v11, v37, v25
	ds_read_b128 v[4:7], v186 offset:9248
	s_add_i32 s1, s1, s19
	s_mov_b32 s14, 0x30000
	s_mov_b32 s15, 0x80000
	s_mov_b32 s19, 0
	s_waitcnt lgkmcnt(2)
	v_mfma_f32_32x32x16_f16 v[82:97], v[14:17], v[130:133], 0
	v_fma_f32 v16, v8, v22, v10
	v_fma_f32 v17, v9, v23, v11
	v_log_f32_e32 v238, v17
	s_nop 0
	v_add_f32_e32 v187, v187, v238
	v_sub_f32_e32 v240, 0, v187
	v_sub_f32_e32 v241, 0, v187
	v_sub_f32_e32 v242, 0, v187
	v_sub_f32_e32 v243, 0, v187
	v_sub_f32_e32 v244, 0, v187
	v_sub_f32_e32 v245, 0, v187
	v_sub_f32_e32 v246, 0, v187
	v_sub_f32_e32 v247, 0, v187
	v_sub_f32_e32 v248, 0, v187
	v_sub_f32_e32 v249, 0, v187
	v_sub_f32_e32 v250, 0, v187
	v_sub_f32_e32 v251, 0, v187
	v_sub_f32_e32 v252, 0, v187
	v_sub_f32_e32 v253, 0, v187
	v_sub_f32_e32 v254, 0, v187
	v_sub_f32_e32 v255, 0, v187
	v_lshrrev_b32_e32 v22, 3, v98
	v_or3_b32 v2, s13, v183, v22
	v_lshlrev_b64 v[8:9], 13, v[2:3]
	v_lshl_add_u64 v[8:9], s[4:5], 0, v[8:9]
	v_lshlrev_b32_e32 v2, 2, v101
	v_lshl_add_u64 v[8:9], v[8:9], 0, v[2:3]
	v_and_b32_e32 v2, 0x70, v54
	v_lshl_add_u64 v[174:175], v[8:9], 0, v[2:3]
	ds_read_b128 v[8:11], v186 offset:64
	s_waitcnt lgkmcnt(2)
	v_mfma_f32_32x32x16_f16 v[66:81], v[18:21], v[118:121], v[66:81]
	v_div_scale_f32 v18, s[4:5], v16, v16, -v41
	v_rcp_f32_e32 v19, v18
	v_div_scale_f32 v20, vcc, -v41, v16, -v41
	s_mov_b32 s13, 0x20000
	v_mov_b32_e32 v24, v3
	s_waitcnt lgkmcnt(1)
	v_mfma_f32_32x32x16_f16 v[82:97], v[4:7], v[134:137], v[82:97]
	v_fma_f32 v4, -v18, v19, 1.0
	v_fmac_f32_e32 v19, v4, v19
	v_mul_f32_e32 v21, v20, v19
	ds_read_b128 v[4:7], v186 offset:9280
	ds_read_b128 v[12:15], v186 offset:96
	v_mov_b32_e32 v25, v3
	v_mov_b32_e32 v26, v3
	v_mov_b32_e32 v27, v3
	s_waitcnt lgkmcnt(2)
	v_mfma_f32_32x32x16_f16 v[66:81], v[8:11], v[122:125], v[66:81]
	v_fma_f32 v8, -v18, v21, v20
	v_fmac_f32_e32 v21, v8, v19
	v_fma_f32 v18, -v18, v21, v20
	v_div_scale_f32 v20, s[4:5], v17, v17, 1.0
	v_rcp_f32_e32 v23, v20
	ds_read_b128 v[8:11], v186 offset:9312
	s_waitcnt lgkmcnt(2)
	v_mfma_f32_32x32x16_f16 v[82:97], v[4:7], v[138:141], v[82:97]
	v_div_fmas_f32 v4, v18, v19, v21
	v_div_fixup_f32 v176, v4, v16, -v41
	v_fma_f32 v4, -v20, v23, 1.0
	v_fmac_f32_e32 v23, v4, v23
	v_div_scale_f32 v4, vcc, 1.0, v17, 1.0
	v_mul_f32_e32 v5, v4, v23
	v_fma_f32 v6, -v20, v5, v4
	v_fmac_f32_e32 v5, v6, v23
	s_waitcnt lgkmcnt(1)
	v_mfma_f32_32x32x16_f16 v[66:81], v[12:15], v[126:129], v[66:81]
	v_fma_f32 v4, -v20, v5, v4
	v_div_fmas_f32 v4, v4, v23, v5
	v_div_fixup_f32 v177, v4, v17, 1.0
	v_mul_u32_u24_e32 v4, 0x90, v22
	v_add3_u32 v189, v40, v4, v2
	v_mul_u32_u24_e32 v2, 0x90, v1
	v_lshlrev_b32_e32 v4, 2, v99
	s_waitcnt lgkmcnt(0)
	v_mfma_f32_32x32x16_f16 v[82:97], v[8:11], v[142:145], v[82:97]
	v_add3_u32 v190, v40, v2, v4
	v_mul_u32_u24_e32 v2, 0x48, v1
	v_lshl_add_u32 v2, v2, 1, 0
	v_lshlrev_b32_e32 v4, 1, v101
	v_add3_u32 v191, v2, v4, v100
	s_mov_b32 s4, 0x3f800000
	s_mov_b32 s5, 0x10000
	v_mov_b32_e32 v2, v3
	v_mov_b32_e32 v4, v3
	v_mov_b32_e32 v5, v3
	v_mov_b32_e32 v6, v3
	v_mov_b32_e32 v7, v3
	v_mov_b32_e32 v8, v3
	v_mov_b32_e32 v9, v3
	v_mov_b32_e32 v10, v3
	v_mov_b32_e32 v11, v3
	v_mov_b32_e32 v12, v3
	v_mov_b32_e32 v13, v3
	v_mov_b32_e32 v14, v3
	v_mov_b32_e32 v15, v3
	v_mov_b32_e32 v16, v3
	v_mov_b32_e32 v17, v3
	v_mov_b32_e32 v18, v3
	v_mov_b32_e32 v19, v3
	v_mov_b32_e32 v20, v3
	v_mov_b32_e32 v21, v3
	v_mov_b32_e32 v22, v3
	v_mov_b32_e32 v23, v3
	v_mov_b32_e32 v28, v3
	v_mov_b32_e32 v29, v3
	v_mov_b32_e32 v30, v3
	v_mov_b32_e32 v31, v3
	v_mov_b32_e32 v32, v3
	v_mov_b32_e32 v33, v3
	v_mov_b32_e32 v34, v3
	v_mov_b32_e32 v35, v3
	v_mov_b32_e32 v36, v3
	v_mov_b32_e32 v37, v3
	v_mov_b32_e32 v38, v3
	v_mov_b32_e32 v39, v3
	v_mov_b32_e32 v40, v3
	v_mov_b32_e32 v41, v3
	v_mov_b32_e32 v42, v3
	v_mov_b32_e32 v43, v3
	v_mov_b32_e32 v44, v3
	v_mov_b32_e32 v45, v3
	v_mov_b32_e32 v46, v3
	v_mov_b32_e32 v47, v3
	v_mov_b32_e32 v48, v3
	v_mov_b32_e32 v49, v3
	v_mov_b32_e32 v50, v3
	v_mov_b32_e32 v51, v3
	v_mov_b32_e32 v52, v3
	v_mov_b32_e32 v53, v3
	v_mov_b32_e32 v54, v3
	v_mov_b32_e32 v56, v3
	v_mov_b32_e32 v57, v3
	v_mov_b32_e32 v58, v3
	v_mov_b32_e32 v59, v3
	v_mov_b32_e32 v60, v3
	v_mov_b32_e32 v61, v3
	v_mov_b32_e32 v62, v3
	v_mov_b32_e32 v63, v3
	v_mov_b32_e32 v64, v3
	v_mov_b32_e32 v65, v3
	v_add_u32_e32 v192, 0xd800, v191
	v_sub_f32_e32 v66, v66, v187
	v_sub_f32_e32 v67, v67, v187
	v_sub_f32_e32 v68, v68, v187
	v_sub_f32_e32 v69, v69, v187
	v_sub_f32_e32 v70, v70, v187
	v_sub_f32_e32 v71, v71, v187
	v_sub_f32_e32 v72, v72, v187
	v_sub_f32_e32 v73, v73, v187
	v_sub_f32_e32 v74, v74, v187
	v_sub_f32_e32 v75, v75, v187
	v_sub_f32_e32 v76, v76, v187
	v_sub_f32_e32 v77, v77, v187
	v_sub_f32_e32 v78, v78, v187
	v_sub_f32_e32 v79, v79, v187
	v_sub_f32_e32 v80, v80, v187
	v_sub_f32_e32 v81, v81, v187
	s_mov_b32 s27, 0x42c80000
	v_cmp_gt_f32_e64 vcc, |v188|, s27
	s_cbranch_vccnz .Ll2_gen
	v_sub_f32_e32 v238, 0, v188
	v_exp_f32_e32 v238, v238
	s_nop 0
	v_mul_f32_e32 v176, v176, v238
	s_barrier
	s_branch .Ll2f_top
